# baseline (speedup 1.0000x reference)
.LBB3_39:
	v_cvt_f16_f32_e32 v3, v14
	v_cvt_f16_f32_e32 v4, v12
	v_mul_f32_e32 v21, v16, v2
	v_fma_mixlo_f16 v5, v16, v2, 0
	v_mul_u32_u24_e32 v16, 0x10001, v3
	v_mul_u32_u24_e32 v22, 0x10001, v4
	v_cvt_f16_f32_e32 v3, v15
	v_cvt_f16_f32_e32 v4, v13
	s_mov_b32 s0, 0x10001
	v_mul_u32_u24_sdwa v23, v5, s0 dst_sel:DWORD dst_unused:UNUSED_PAD src0_sel:WORD_0 src1_sel:DWORD
	v_mul_f32_e32 v24, v17, v2
	v_fma_mixlo_f16 v5, v17, v2, 0
	v_mul_u32_u24_e32 v17, 0x10001, v3
	v_mul_u32_u24_e32 v25, 0x10001, v4
	v_cvt_f16_f32_e32 v3, v8
	v_cvt_f16_f32_e32 v4, v6
	v_mul_u32_u24_sdwa v26, v5, s0 dst_sel:DWORD dst_unused:UNUSED_PAD src0_sel:WORD_0 src1_sel:DWORD
	v_mul_f32_e32 v27, v10, v2
	v_fma_mixlo_f16 v5, v10, v2, 0
	v_mul_u32_u24_e32 v10, 0x10001, v3
	v_mul_u32_u24_e32 v28, 0x10001, v4
	v_cvt_f16_f32_e32 v3, v9
	v_cvt_f16_f32_e32 v4, v7
	v_sub_u32_e32 v20, 0x7f000000, v2
	v_mul_f32_e32 v14, v14, v2
	v_mul_f32_e32 v12, v12, v2
	v_mul_f32_e32 v15, v15, v2
	v_mul_f32_e32 v13, v13, v2
	v_mul_u32_u24_sdwa v29, v5, s0 dst_sel:DWORD dst_unused:UNUSED_PAD src0_sel:WORD_0 src1_sel:DWORD
	v_mul_f32_e32 v8, v8, v2
	v_mul_f32_e32 v6, v6, v2
	v_mul_f32_e32 v30, v11, v2
	v_fma_mixlo_f16 v5, v11, v2, 0
	v_mul_f32_e32 v9, v9, v2
	v_mul_f32_e32 v7, v7, v2
	v_cndmask_b32_e64 v2, 0, 1, s[26:27]
	v_mul_u32_u24_e32 v11, 0x10001, v3
	v_mul_u32_u24_e32 v31, 0x10001, v4
	v_mul_u32_u24_sdwa v32, v5, s0 dst_sel:DWORD dst_unused:UNUSED_PAD src0_sel:WORD_0 src1_sel:DWORD
	v_lshlrev_b32_e32 v33, 1, v33
	v_mov_b32_e32 v34, 0x22c50
	v_cmp_ne_u32_e64 s[6:7], 1, v2
	s_movk_i32 s12, 0x3c00
	v_mov_b32_e32 v35, 0x3c00
	s_sub_i32 s34, 0xe0, s3
	s_mul_i32 s35, s34, 33
	s_mul_i32 s36, s3, 0x210
	v_mov_b32_e32 v68, 0
	v_mov_b32_e32 v69, 0
	v_mov_b32_e32 v70, 0
	v_mov_b32_e32 v71, 0
	v_mov_b32_e32 v72, v0
	v_lshlrev_b32_e32 v73, 4, v0
	v_add_u32_e32 v73, s36, v73
	s_mov_b64 s[36:37], exec
.Lz_loop:
	v_cmp_gt_u32_e32 vcc, s35, v72
	s_and_b64 exec, exec, vcc
	s_cbranch_execz .Lz_done
	ds_write_b128 v73, v[68:71]
	v_add_u32_e32 v72, 0x400, v72
	v_add_u32_e32 v73, 0x4000, v73
	s_branch .Lz_loop
.Lz_done:
	s_mov_b64 exec, s[36:37]
	v_cmp_gt_u32_e32 vcc, s34, v0
	v_add_u32_e32 v73, s3, v0
	v_lshlrev_b32_e32 v73, 2, v73
	v_add_u32_e32 v73, 0x22200, v73
	s_and_saveexec_b64 s[36:37], vcc
	ds_write_b32 v73, v68
	s_mov_b64 exec, s[36:37]
	s_movk_i32 s34, 0x100
	v_cmp_gt_u32_e32 vcc, s34, v0
	s_and_saveexec_b64 s[34:35], vcc
	s_cbranch_execz .Lskip_stage
	s_waitcnt vmcnt(0)
	v_cvt_pk_f16_f32 v64, v64, v65
	v_lshlrev_b32_e32 v63, 2, v0
	v_add_u32_e32 v63, 0x24870, v63
	ds_write_b32 v63, v64
	ds_write_b32 v63, v66 offset:1024

.LBB3_99:
	s_or_b64 exec, exec, s[0:1]
	v_lshl_or_b32 v56, v105, 5, v106
	v_lshlrev_b32_e32 v54, 2, v56
	global_load_dword v59, v54, s[72:73]
	global_load_dword v60, v54, s[72:73] offset:64
	v_and_b32_e32 v57, 0x8c, v103
	v_mov_b32_e32 v58, 0x22200
	v_lshl_add_u32 v58, v57, 2, v58
	ds_read_b128 v[74:77], v58 offset:0
	ds_read_b128 v[78:81], v58 offset:64
	ds_read_b128 v[82:85], v58 offset:128
	ds_read_b128 v[86:89], v58 offset:192
	ds_read_b128 v[90:93], v58 offset:256
	ds_read_b128 v[94:97], v58 offset:320
	v_sub_u32_e32 v98, s3, v57
	v_mov_b32_e32 v99, 0
	v_add_u32_e32 v107, 0, v98
	v_med3_i32 v107, v107, 0, 4
	v_add_u32_e32 v99, v99, v107
	v_add_u32_e32 v107, -16, v98
	v_med3_i32 v107, v107, 0, 4
	v_add_u32_e32 v99, v99, v107
	v_add_u32_e32 v107, -32, v98
	v_med3_i32 v107, v107, 0, 4
	v_add_u32_e32 v99, v99, v107
	v_add_u32_e32 v107, -48, v98
	v_med3_i32 v107, v107, 0, 4
	v_add_u32_e32 v99, v99, v107
	v_add_u32_e32 v107, -64, v98
	v_med3_i32 v107, v107, 0, 4
	v_add_u32_e32 v99, v99, v107
	v_add_u32_e32 v107, -80, v98
	v_med3_i32 v107, v107, 0, 4
	v_add_u32_e32 v99, v99, v107
	v_mov_b32_e32 v100, 0
	v_mov_b32_e32 v101, 0
	v_mov_b32_e32 v55, 24
	s_waitcnt vmcnt(0)
	s_waitcnt lgkmcnt(5)
	v_fma_f32 v108, v66, v74, v59
	v_fma_f32 v109, v30, v74, v60
	v_max_f32_e32 v108, 0, v108
	v_max_f32_e32 v109, 0, v109
	v_add_f32_e32 v100, v100, v108
	v_add_f32_e32 v101, v101, v109
	v_fma_f32 v108, v67, v75, v59
	v_fma_f32 v109, v31, v75, v60
	v_max_f32_e32 v108, 0, v108
	v_max_f32_e32 v109, 0, v109
	v_add_f32_e32 v100, v100, v108
	v_add_f32_e32 v101, v101, v109
	v_fma_f32 v108, v68, v76, v59
	v_fma_f32 v109, v32, v76, v60
	v_max_f32_e32 v108, 0, v108
	v_max_f32_e32 v109, 0, v109
	v_add_f32_e32 v100, v100, v108
	v_add_f32_e32 v101, v101, v109
	v_fma_f32 v108, v69, v77, v59
	v_fma_f32 v109, v33, v77, v60
	v_max_f32_e32 v108, 0, v108
	v_max_f32_e32 v109, 0, v109
	v_add_f32_e32 v100, v100, v108
	v_add_f32_e32 v101, v101, v109
	s_waitcnt lgkmcnt(4)
	v_fma_f32 v108, v62, v78, v59
	v_fma_f32 v109, v22, v78, v60
	v_max_f32_e32 v108, 0, v108
	v_max_f32_e32 v109, 0, v109
	v_add_f32_e32 v100, v100, v108
	v_add_f32_e32 v101, v101, v109
	v_fma_f32 v108, v63, v79, v59
	v_fma_f32 v109, v23, v79, v60
	v_max_f32_e32 v108, 0, v108
	v_max_f32_e32 v109, 0, v109
	v_add_f32_e32 v100, v100, v108
	v_add_f32_e32 v101, v101, v109
	v_fma_f32 v108, v64, v80, v59
	v_fma_f32 v109, v24, v80, v60
	v_max_f32_e32 v108, 0, v108
	v_max_f32_e32 v109, 0, v109
	v_add_f32_e32 v100, v100, v108
	v_add_f32_e32 v101, v101, v109
	v_fma_f32 v108, v65, v81, v59
	v_fma_f32 v109, v25, v81, v60
	v_max_f32_e32 v108, 0, v108
	v_max_f32_e32 v109, 0, v109
	v_add_f32_e32 v100, v100, v108
	v_add_f32_e32 v101, v101, v109
	s_waitcnt lgkmcnt(3)
	v_fma_f32 v108, v70, v82, v59
	v_fma_f32 v109, v34, v82, v60
	v_max_f32_e32 v108, 0, v108
	v_max_f32_e32 v109, 0, v109
	v_add_f32_e32 v100, v100, v108
	v_add_f32_e32 v101, v101, v109
	v_fma_f32 v108, v71, v83, v59
	v_fma_f32 v109, v35, v83, v60
	v_max_f32_e32 v108, 0, v108
	v_max_f32_e32 v109, 0, v109
	v_add_f32_e32 v100, v100, v108
	v_add_f32_e32 v101, v101, v109
	v_fma_f32 v108, v72, v84, v59
	v_fma_f32 v109, v36, v84, v60
	v_max_f32_e32 v108, 0, v108
	v_max_f32_e32 v109, 0, v109
	v_add_f32_e32 v100, v100, v108
	v_add_f32_e32 v101, v101, v109
	v_fma_f32 v108, v73, v85, v59
	v_fma_f32 v109, v37, v85, v60
	v_max_f32_e32 v108, 0, v108
	v_max_f32_e32 v109, 0, v109
	v_add_f32_e32 v100, v100, v108
	v_add_f32_e32 v101, v101, v109
	s_waitcnt lgkmcnt(2)
	v_fma_f32 v108, v50, v86, v59
	v_fma_f32 v109, v26, v86, v60
	v_max_f32_e32 v108, 0, v108
	v_max_f32_e32 v109, 0, v109
	v_add_f32_e32 v100, v100, v108
	v_add_f32_e32 v101, v101, v109
	v_fma_f32 v108, v51, v87, v59
	v_fma_f32 v109, v27, v87, v60
	v_max_f32_e32 v108, 0, v108
	v_max_f32_e32 v109, 0, v109
	v_add_f32_e32 v100, v100, v108
	v_add_f32_e32 v101, v101, v109
	v_fma_f32 v108, v52, v88, v59
	v_fma_f32 v109, v28, v88, v60
	v_max_f32_e32 v108, 0, v108
	v_max_f32_e32 v109, 0, v109
	v_add_f32_e32 v100, v100, v108
	v_add_f32_e32 v101, v101, v109
	v_fma_f32 v108, v53, v89, v59
	v_fma_f32 v109, v29, v89, v60
	v_max_f32_e32 v108, 0, v108
	v_max_f32_e32 v109, 0, v109
	v_add_f32_e32 v100, v100, v108
	v_add_f32_e32 v101, v101, v109
	s_waitcnt lgkmcnt(1)
	v_fma_f32 v108, v46, v90, v59
	v_fma_f32 v109, v38, v90, v60
	v_max_f32_e32 v108, 0, v108
	v_max_f32_e32 v109, 0, v109
	v_add_f32_e32 v100, v100, v108
	v_add_f32_e32 v101, v101, v109
	v_fma_f32 v108, v47, v91, v59
	v_fma_f32 v109, v39, v91, v60
	v_max_f32_e32 v108, 0, v108
	v_max_f32_e32 v109, 0, v109
	v_add_f32_e32 v100, v100, v108
	v_add_f32_e32 v101, v101, v109
	v_fma_f32 v108, v48, v92, v59
	v_fma_f32 v109, v40, v92, v60
	v_max_f32_e32 v108, 0, v108
	v_max_f32_e32 v109, 0, v109
	v_add_f32_e32 v100, v100, v108
	v_add_f32_e32 v101, v101, v109
	v_fma_f32 v108, v49, v93, v59
	v_fma_f32 v109, v41, v93, v60
	v_max_f32_e32 v108, 0, v108
	v_max_f32_e32 v109, 0, v109
	v_add_f32_e32 v100, v100, v108
	v_add_f32_e32 v101, v101, v109
	s_waitcnt lgkmcnt(0)
	v_fma_f32 v108, v42, v94, v59
	v_fma_f32 v109, v18, v94, v60
	v_max_f32_e32 v108, 0, v108
	v_max_f32_e32 v109, 0, v109
	v_add_f32_e32 v100, v100, v108
	v_add_f32_e32 v101, v101, v109
	v_fma_f32 v108, v43, v95, v59
	v_fma_f32 v109, v19, v95, v60
	v_max_f32_e32 v108, 0, v108
	v_max_f32_e32 v109, 0, v109
	v_add_f32_e32 v100, v100, v108
	v_add_f32_e32 v101, v101, v109
	v_fma_f32 v108, v44, v96, v59
	v_fma_f32 v109, v20, v96, v60
	v_max_f32_e32 v108, 0, v108
	v_max_f32_e32 v109, 0, v109
	v_add_f32_e32 v100, v100, v108
	v_add_f32_e32 v101, v101, v109
	v_fma_f32 v108, v45, v97, v59
	v_fma_f32 v109, v21, v97, v60
	v_max_f32_e32 v108, 0, v108
	v_max_f32_e32 v109, 0, v109
	v_add_f32_e32 v100, v100, v108
	v_add_f32_e32 v101, v101, v109
	s_and_b64 vcc, exec, s[4:5]
	s_cbranch_vccz .Lepi_tail
	ds_read_b128 v[74:77], v58 offset:384
	ds_read_b128 v[78:81], v58 offset:448
	v_add_u32_e32 v107, -96, v98
	v_med3_i32 v107, v107, 0, 4
	v_add_u32_e32 v99, v99, v107
	v_add_u32_e32 v107, -112, v98
	v_med3_i32 v107, v107, 0, 4
	v_add_u32_e32 v99, v99, v107
	v_mov_b32_e32 v55, 32
	s_waitcnt lgkmcnt(1)
	v_fma_f32 v108, v14, v74, v59
	v_fma_f32 v109, v6, v74, v60
	v_max_f32_e32 v108, 0, v108
	v_max_f32_e32 v109, 0, v109
	v_add_f32_e32 v100, v100, v108
	v_add_f32_e32 v101, v101, v109
	v_fma_f32 v108, v15, v75, v59
	v_fma_f32 v109, v7, v75, v60
	v_max_f32_e32 v108, 0, v108
	v_max_f32_e32 v109, 0, v109
	v_add_f32_e32 v100, v100, v108
	v_add_f32_e32 v101, v101, v109
	v_fma_f32 v108, v16, v76, v59
	v_fma_f32 v109, v8, v76, v60
	v_max_f32_e32 v108, 0, v108
	v_max_f32_e32 v109, 0, v109
	v_add_f32_e32 v100, v100, v108
	v_add_f32_e32 v101, v101, v109
	v_fma_f32 v108, v17, v77, v59
	v_fma_f32 v109, v9, v77, v60
	v_max_f32_e32 v108, 0, v108
	v_max_f32_e32 v109, 0, v109
	v_add_f32_e32 v100, v100, v108
	v_add_f32_e32 v101, v101, v109
	s_waitcnt lgkmcnt(0)
	v_fma_f32 v108, v10, v78, v59
	v_fma_f32 v109, v2, v78, v60
	v_max_f32_e32 v108, 0, v108
	v_max_f32_e32 v109, 0, v109
	v_add_f32_e32 v100, v100, v108
	v_add_f32_e32 v101, v101, v109
	v_fma_f32 v108, v11, v79, v59
	v_fma_f32 v109, v3, v79, v60
	v_max_f32_e32 v108, 0, v108
	v_max_f32_e32 v109, 0, v109
	v_add_f32_e32 v100, v100, v108
	v_add_f32_e32 v101, v101, v109
	v_fma_f32 v108, v12, v80, v59
	v_fma_f32 v109, v4, v80, v60
	v_max_f32_e32 v108, 0, v108
	v_max_f32_e32 v109, 0, v109
	v_add_f32_e32 v100, v100, v108
	v_add_f32_e32 v101, v101, v109
	v_fma_f32 v108, v13, v81, v59
	v_fma_f32 v109, v5, v81, v60
	v_max_f32_e32 v108, 0, v108
	v_max_f32_e32 v109, 0, v109
	v_add_f32_e32 v100, v100, v108
	v_add_f32_e32 v101, v101, v109
.Lepi_tail:
	v_sub_u32_e32 v99, v55, v99
	v_cvt_f32_i32_e32 v99, v99
	v_max_f32_e32 v108, 0, v59
	v_max_f32_e32 v109, 0, v60
	v_fma_f32 v100, -v99, v108, v100
	v_fma_f32 v101, -v99, v109, v101
	v_mov_b32_e32 v3, 0x21e00
	v_lshl_add_u32 v3, v56, 2, v3
	ds_add_f32 v3, v100
	ds_add_f32 v3, v101 offset:64
	s_mov_b64 s[0:1], exec
